# P7 epilogue: packed dword per row, quad transpose, then ds_bpermute so that lanes hold consecutive dwords: 16 fully coalesced global_store_dword per lane (2 x 128 B per instruction) instead of 64 byte
# baseline (speedup 1.0000x reference)
.LBB0_1720:
	s_or_b64 exec, exec, s[6:7]
	s_waitcnt lgkmcnt(0)
	s_mov_b64 s[26:27], 0
	ds_read_b128 v[120:123], v198
	ds_read_b128 v[124:127], v198 offset:32
	ds_read_b128 v[128:131], v198 offset:64
	ds_read_b128 v[132:135], v198 offset:96
	v_and_b32_e32 v86, 3, v0
	v_mul_u32_u24_e32 v136, 0x101, v86
	v_add_u32_e32 v136, 0xc0c0400, v136
	v_and_b32_e32 v84, 31, v0
	v_mul_u32_u24_e32 v86, 3, v84
	v_and_b32_e32 v85, 7, v0
	v_bfe_u32 v84, v0, 3, 2
	v_lshl_add_u32 v84, v85, 2, v84
	v_and_or_b32 v84, v0, 32, v84
	v_lshlrev_b32_e32 v84, 2, v84
	v_mov_b32_e32 v87, 0
	v_lshl_add_u64 v[74:75], v[178:179], 0, s[24:25]
	v_lshlrev_b32_e32 v137, 16, v136
	v_or_b32_e32 v137, 0xc0c, v137
	v_lshl_add_u64 v[74:75], v[74:75], 0, v[86:87]
	v_add_co_u32_e32 v76, vcc, s41, v74
	s_nop 1
	v_addc_co_u32_e32 v77, vcc, 0, v75, vcc
	v_add_co_u32_e32 v78, vcc, s30, v74
	s_nop 1
	v_addc_co_u32_e32 v79, vcc, 0, v75, vcc
	v_add_co_u32_e32 v80, vcc, s42, v74
	s_nop 1
	v_addc_co_u32_e32 v81, vcc, 0, v75, vcc
	s_waitcnt lgkmcnt(3)
	v_rcp_f32_e32 v104, v120
	v_rcp_f32_e32 v105, v121
	v_rcp_f32_e32 v106, v122
	v_rcp_f32_e32 v107, v123
	s_waitcnt lgkmcnt(2)
	v_rcp_f32_e32 v108, v124
	v_rcp_f32_e32 v109, v125
	v_rcp_f32_e32 v110, v126
	v_rcp_f32_e32 v111, v127
	s_waitcnt lgkmcnt(1)
	v_rcp_f32_e32 v112, v128
	v_rcp_f32_e32 v113, v129
	v_rcp_f32_e32 v114, v130
	v_rcp_f32_e32 v115, v131
	s_waitcnt lgkmcnt(0)
	v_rcp_f32_e32 v116, v132
	v_rcp_f32_e32 v117, v133
	v_rcp_f32_e32 v118, v134
	v_rcp_f32_e32 v119, v135
	s_nop 0
	v_mul_f32_e32 v138, v50, v104
	v_mul_f32_e32 v139, v34, v104
	v_mul_f32_e32 v140, v18, v104
	v_mul_f32_e32 v141, v2, v104
	v_mul_f32_e32 v138, 0x42000000, v138
	v_mul_f32_e32 v139, 0x42000000, v139
	v_mul_f32_e32 v140, 0x42000000, v140
	v_mul_f32_e32 v141, 0x42000000, v141
	v_med3_f32 v138, v138, s40, v212
	v_med3_f32 v139, v139, s40, v212
	v_med3_f32 v140, v140, s40, v212
	v_med3_f32 v141, v141, s40, v212
	v_cvt_pk_fp8_f32 v142, v138, v139
	v_cvt_pk_fp8_f32 v142, v140, v141 op_sel:[0,0,1]
	v_mul_f32_e32 v138, v51, v105
	v_mul_f32_e32 v139, v35, v105
	v_mul_f32_e32 v140, v19, v105
	v_mul_f32_e32 v141, v3, v105
	v_mul_f32_e32 v138, 0x42000000, v138
	v_mul_f32_e32 v139, 0x42000000, v139
	v_mul_f32_e32 v140, 0x42000000, v140
	v_mul_f32_e32 v141, 0x42000000, v141
	v_med3_f32 v138, v138, s40, v212
	v_med3_f32 v139, v139, s40, v212
	v_med3_f32 v140, v140, s40, v212
	v_med3_f32 v141, v141, s40, v212
	v_cvt_pk_fp8_f32 v143, v138, v139
	v_cvt_pk_fp8_f32 v143, v140, v141 op_sel:[0,0,1]
	v_mov_b32_dpp v66, v142 quad_perm:[0,0,0,0] row_mask:0xf bank_mask:0xf
	v_mov_b32_dpp v67, v142 quad_perm:[1,1,1,1] row_mask:0xf bank_mask:0xf
	v_mov_b32_dpp v68, v142 quad_perm:[2,2,2,2] row_mask:0xf bank_mask:0xf
	v_mov_b32_dpp v69, v142 quad_perm:[3,3,3,3] row_mask:0xf bank_mask:0xf
	s_nop 0
	v_perm_b32 v70, v67, v66, v136
	v_perm_b32 v71, v69, v68, v137
	v_or_b32_e32 v72, v70, v71
	ds_bpermute_b32 v213, v84, v72
	v_mul_f32_e32 v138, v52, v106
	v_mul_f32_e32 v139, v36, v106
	v_mul_f32_e32 v140, v20, v106
	v_mul_f32_e32 v141, v4, v106
	v_mul_f32_e32 v138, 0x42000000, v138
	v_mul_f32_e32 v139, 0x42000000, v139
	v_mul_f32_e32 v140, 0x42000000, v140
	v_mul_f32_e32 v141, 0x42000000, v141
	v_med3_f32 v138, v138, s40, v212
	v_med3_f32 v139, v139, s40, v212
	v_med3_f32 v140, v140, s40, v212
	v_med3_f32 v141, v141, s40, v212
	v_cvt_pk_fp8_f32 v142, v138, v139
	v_cvt_pk_fp8_f32 v142, v140, v141 op_sel:[0,0,1]
	v_mov_b32_dpp v66, v143 quad_perm:[0,0,0,0] row_mask:0xf bank_mask:0xf
	v_mov_b32_dpp v67, v143 quad_perm:[1,1,1,1] row_mask:0xf bank_mask:0xf
	v_mov_b32_dpp v68, v143 quad_perm:[2,2,2,2] row_mask:0xf bank_mask:0xf
	v_mov_b32_dpp v69, v143 quad_perm:[3,3,3,3] row_mask:0xf bank_mask:0xf
	s_nop 0
	v_perm_b32 v70, v67, v66, v136
	v_perm_b32 v71, v69, v68, v137
	v_or_b32_e32 v72, v70, v71
	ds_bpermute_b32 v214, v84, v72
	s_waitcnt lgkmcnt(1)
	global_store_dword v[74:75], v213, off
	v_mul_f32_e32 v138, v53, v107
	v_mul_f32_e32 v139, v37, v107
	v_mul_f32_e32 v140, v21, v107
	v_mul_f32_e32 v141, v5, v107
	v_mul_f32_e32 v138, 0x42000000, v138
	v_mul_f32_e32 v139, 0x42000000, v139
	v_mul_f32_e32 v140, 0x42000000, v140
	v_mul_f32_e32 v141, 0x42000000, v141
	v_med3_f32 v138, v138, s40, v212
	v_med3_f32 v139, v139, s40, v212
	v_med3_f32 v140, v140, s40, v212
	v_med3_f32 v141, v141, s40, v212
	v_cvt_pk_fp8_f32 v143, v138, v139
	v_cvt_pk_fp8_f32 v143, v140, v141 op_sel:[0,0,1]
	v_mov_b32_dpp v66, v142 quad_perm:[0,0,0,0] row_mask:0xf bank_mask:0xf
	v_mov_b32_dpp v67, v142 quad_perm:[1,1,1,1] row_mask:0xf bank_mask:0xf
	v_mov_b32_dpp v68, v142 quad_perm:[2,2,2,2] row_mask:0xf bank_mask:0xf
	v_mov_b32_dpp v69, v142 quad_perm:[3,3,3,3] row_mask:0xf bank_mask:0xf
	s_nop 0
	v_perm_b32 v70, v67, v66, v136
	v_perm_b32 v71, v69, v68, v137
	v_or_b32_e32 v72, v70, v71
	ds_bpermute_b32 v215, v84, v72
	s_waitcnt lgkmcnt(1)
	global_store_dword v[74:75], v214, off offset:1024
	v_mul_f32_e32 v138, v54, v108
	v_mul_f32_e32 v139, v38, v108
	v_mul_f32_e32 v140, v22, v108
	v_mul_f32_e32 v141, v6, v108
	v_mul_f32_e32 v138, 0x42000000, v138
	v_mul_f32_e32 v139, 0x42000000, v139
	v_mul_f32_e32 v140, 0x42000000, v140
	v_mul_f32_e32 v141, 0x42000000, v141
	v_med3_f32 v138, v138, s40, v212
	v_med3_f32 v139, v139, s40, v212
	v_med3_f32 v140, v140, s40, v212
	v_med3_f32 v141, v141, s40, v212
	v_cvt_pk_fp8_f32 v142, v138, v139
	v_cvt_pk_fp8_f32 v142, v140, v141 op_sel:[0,0,1]
	v_mov_b32_dpp v66, v143 quad_perm:[0,0,0,0] row_mask:0xf bank_mask:0xf
	v_mov_b32_dpp v67, v143 quad_perm:[1,1,1,1] row_mask:0xf bank_mask:0xf
	v_mov_b32_dpp v68, v143 quad_perm:[2,2,2,2] row_mask:0xf bank_mask:0xf
	v_mov_b32_dpp v69, v143 quad_perm:[3,3,3,3] row_mask:0xf bank_mask:0xf
	s_nop 0
	v_perm_b32 v70, v67, v66, v136
	v_perm_b32 v71, v69, v68, v137
	v_or_b32_e32 v72, v70, v71
	ds_bpermute_b32 v216, v84, v72
	s_waitcnt lgkmcnt(1)
	global_store_dword v[74:75], v215, off offset:2048
	v_mul_f32_e32 v138, v55, v109
	v_mul_f32_e32 v139, v39, v109
	v_mul_f32_e32 v140, v23, v109
	v_mul_f32_e32 v141, v7, v109
	v_mul_f32_e32 v138, 0x42000000, v138
	v_mul_f32_e32 v139, 0x42000000, v139
	v_mul_f32_e32 v140, 0x42000000, v140
	v_mul_f32_e32 v141, 0x42000000, v141
	v_med3_f32 v138, v138, s40, v212
	v_med3_f32 v139, v139, s40, v212
	v_med3_f32 v140, v140, s40, v212
	v_med3_f32 v141, v141, s40, v212
	v_cvt_pk_fp8_f32 v143, v138, v139
	v_cvt_pk_fp8_f32 v143, v140, v141 op_sel:[0,0,1]
	v_mov_b32_dpp v66, v142 quad_perm:[0,0,0,0] row_mask:0xf bank_mask:0xf
	v_mov_b32_dpp v67, v142 quad_perm:[1,1,1,1] row_mask:0xf bank_mask:0xf
	v_mov_b32_dpp v68, v142 quad_perm:[2,2,2,2] row_mask:0xf bank_mask:0xf
	v_mov_b32_dpp v69, v142 quad_perm:[3,3,3,3] row_mask:0xf bank_mask:0xf
	s_nop 0
	v_perm_b32 v70, v67, v66, v136
	v_perm_b32 v71, v69, v68, v137
	v_or_b32_e32 v72, v70, v71
	ds_bpermute_b32 v217, v84, v72
	s_waitcnt lgkmcnt(1)
	global_store_dword v[74:75], v216, off offset:3072
	v_mul_f32_e32 v138, v56, v110
	v_mul_f32_e32 v139, v40, v110
	v_mul_f32_e32 v140, v24, v110
	v_mul_f32_e32 v141, v8, v110
	v_mul_f32_e32 v138, 0x42000000, v138
	v_mul_f32_e32 v139, 0x42000000, v139
	v_mul_f32_e32 v140, 0x42000000, v140
	v_mul_f32_e32 v141, 0x42000000, v141
	v_med3_f32 v138, v138, s40, v212
	v_med3_f32 v139, v139, s40, v212
	v_med3_f32 v140, v140, s40, v212
	v_med3_f32 v141, v141, s40, v212
	v_cvt_pk_fp8_f32 v142, v138, v139
	v_cvt_pk_fp8_f32 v142, v140, v141 op_sel:[0,0,1]
	v_mov_b32_dpp v66, v143 quad_perm:[0,0,0,0] row_mask:0xf bank_mask:0xf
	v_mov_b32_dpp v67, v143 quad_perm:[1,1,1,1] row_mask:0xf bank_mask:0xf
	v_mov_b32_dpp v68, v143 quad_perm:[2,2,2,2] row_mask:0xf bank_mask:0xf
	v_mov_b32_dpp v69, v143 quad_perm:[3,3,3,3] row_mask:0xf bank_mask:0xf
	s_nop 0
	v_perm_b32 v70, v67, v66, v136
	v_perm_b32 v71, v69, v68, v137
	v_or_b32_e32 v72, v70, v71
	ds_bpermute_b32 v218, v84, v72
	s_waitcnt lgkmcnt(1)
	global_store_dword v[76:77], v217, off
	v_mul_f32_e32 v138, v57, v111
	v_mul_f32_e32 v139, v41, v111
	v_mul_f32_e32 v140, v25, v111
	v_mul_f32_e32 v141, v9, v111
	v_mul_f32_e32 v138, 0x42000000, v138
	v_mul_f32_e32 v139, 0x42000000, v139
	v_mul_f32_e32 v140, 0x42000000, v140
	v_mul_f32_e32 v141, 0x42000000, v141
	v_med3_f32 v138, v138, s40, v212
	v_med3_f32 v139, v139, s40, v212
	v_med3_f32 v140, v140, s40, v212
	v_med3_f32 v141, v141, s40, v212
	v_cvt_pk_fp8_f32 v143, v138, v139
	v_cvt_pk_fp8_f32 v143, v140, v141 op_sel:[0,0,1]
	v_mov_b32_dpp v66, v142 quad_perm:[0,0,0,0] row_mask:0xf bank_mask:0xf
	v_mov_b32_dpp v67, v142 quad_perm:[1,1,1,1] row_mask:0xf bank_mask:0xf
	v_mov_b32_dpp v68, v142 quad_perm:[2,2,2,2] row_mask:0xf bank_mask:0xf
	v_mov_b32_dpp v69, v142 quad_perm:[3,3,3,3] row_mask:0xf bank_mask:0xf
	s_nop 0
	v_perm_b32 v70, v67, v66, v136
	v_perm_b32 v71, v69, v68, v137
	v_or_b32_e32 v72, v70, v71
	ds_bpermute_b32 v219, v84, v72
	s_waitcnt lgkmcnt(1)
	global_store_dword v[76:77], v218, off offset:1024
	v_mul_f32_e32 v138, v58, v112
	v_mul_f32_e32 v139, v42, v112
	v_mul_f32_e32 v140, v26, v112
	v_mul_f32_e32 v141, v10, v112
	v_mul_f32_e32 v138, 0x42000000, v138
	v_mul_f32_e32 v139, 0x42000000, v139
	v_mul_f32_e32 v140, 0x42000000, v140
	v_mul_f32_e32 v141, 0x42000000, v141
	v_med3_f32 v138, v138, s40, v212
	v_med3_f32 v139, v139, s40, v212
	v_med3_f32 v140, v140, s40, v212
	v_med3_f32 v141, v141, s40, v212
	v_cvt_pk_fp8_f32 v142, v138, v139
	v_cvt_pk_fp8_f32 v142, v140, v141 op_sel:[0,0,1]
	v_mov_b32_dpp v66, v143 quad_perm:[0,0,0,0] row_mask:0xf bank_mask:0xf
	v_mov_b32_dpp v67, v143 quad_perm:[1,1,1,1] row_mask:0xf bank_mask:0xf
	v_mov_b32_dpp v68, v143 quad_perm:[2,2,2,2] row_mask:0xf bank_mask:0xf
	v_mov_b32_dpp v69, v143 quad_perm:[3,3,3,3] row_mask:0xf bank_mask:0xf
	s_nop 0
	v_perm_b32 v70, v67, v66, v136
	v_perm_b32 v71, v69, v68, v137
	v_or_b32_e32 v72, v70, v71
	ds_bpermute_b32 v220, v84, v72
	s_waitcnt lgkmcnt(1)
	global_store_dword v[76:77], v219, off offset:2048
	v_mul_f32_e32 v138, v59, v113
	v_mul_f32_e32 v139, v43, v113
	v_mul_f32_e32 v140, v27, v113
	v_mul_f32_e32 v141, v11, v113
	v_mul_f32_e32 v138, 0x42000000, v138
	v_mul_f32_e32 v139, 0x42000000, v139
	v_mul_f32_e32 v140, 0x42000000, v140
	v_mul_f32_e32 v141, 0x42000000, v141
	v_med3_f32 v138, v138, s40, v212
	v_med3_f32 v139, v139, s40, v212
	v_med3_f32 v140, v140, s40, v212
	v_med3_f32 v141, v141, s40, v212
	v_cvt_pk_fp8_f32 v143, v138, v139
	v_cvt_pk_fp8_f32 v143, v140, v141 op_sel:[0,0,1]
	v_mov_b32_dpp v66, v142 quad_perm:[0,0,0,0] row_mask:0xf bank_mask:0xf
	v_mov_b32_dpp v67, v142 quad_perm:[1,1,1,1] row_mask:0xf bank_mask:0xf
	v_mov_b32_dpp v68, v142 quad_perm:[2,2,2,2] row_mask:0xf bank_mask:0xf
	v_mov_b32_dpp v69, v142 quad_perm:[3,3,3,3] row_mask:0xf bank_mask:0xf
	s_nop 0
	v_perm_b32 v70, v67, v66, v136
	v_perm_b32 v71, v69, v68, v137
	v_or_b32_e32 v72, v70, v71
	ds_bpermute_b32 v221, v84, v72
	s_waitcnt lgkmcnt(1)
	global_store_dword v[76:77], v220, off offset:3072
	v_mul_f32_e32 v138, v60, v114
	v_mul_f32_e32 v139, v44, v114
	v_mul_f32_e32 v140, v28, v114
	v_mul_f32_e32 v141, v12, v114
	v_mul_f32_e32 v138, 0x42000000, v138
	v_mul_f32_e32 v139, 0x42000000, v139
	v_mul_f32_e32 v140, 0x42000000, v140
	v_mul_f32_e32 v141, 0x42000000, v141
	v_med3_f32 v138, v138, s40, v212
	v_med3_f32 v139, v139, s40, v212
	v_med3_f32 v140, v140, s40, v212
	v_med3_f32 v141, v141, s40, v212
	v_cvt_pk_fp8_f32 v142, v138, v139
	v_cvt_pk_fp8_f32 v142, v140, v141 op_sel:[0,0,1]
	v_mov_b32_dpp v66, v143 quad_perm:[0,0,0,0] row_mask:0xf bank_mask:0xf
	v_mov_b32_dpp v67, v143 quad_perm:[1,1,1,1] row_mask:0xf bank_mask:0xf
	v_mov_b32_dpp v68, v143 quad_perm:[2,2,2,2] row_mask:0xf bank_mask:0xf
	v_mov_b32_dpp v69, v143 quad_perm:[3,3,3,3] row_mask:0xf bank_mask:0xf
	s_nop 0
	v_perm_b32 v70, v67, v66, v136
	v_perm_b32 v71, v69, v68, v137
	v_or_b32_e32 v72, v70, v71
	ds_bpermute_b32 v222, v84, v72
	s_waitcnt lgkmcnt(1)
	global_store_dword v[78:79], v221, off
	v_mul_f32_e32 v138, v61, v115
	v_mul_f32_e32 v139, v45, v115
	v_mul_f32_e32 v140, v29, v115
	v_mul_f32_e32 v141, v13, v115
	v_mul_f32_e32 v138, 0x42000000, v138
	v_mul_f32_e32 v139, 0x42000000, v139
	v_mul_f32_e32 v140, 0x42000000, v140
	v_mul_f32_e32 v141, 0x42000000, v141
	v_med3_f32 v138, v138, s40, v212
	v_med3_f32 v139, v139, s40, v212
	v_med3_f32 v140, v140, s40, v212
	v_med3_f32 v141, v141, s40, v212
	v_cvt_pk_fp8_f32 v143, v138, v139
	v_cvt_pk_fp8_f32 v143, v140, v141 op_sel:[0,0,1]
	v_mov_b32_dpp v66, v142 quad_perm:[0,0,0,0] row_mask:0xf bank_mask:0xf
	v_mov_b32_dpp v67, v142 quad_perm:[1,1,1,1] row_mask:0xf bank_mask:0xf
	v_mov_b32_dpp v68, v142 quad_perm:[2,2,2,2] row_mask:0xf bank_mask:0xf
	v_mov_b32_dpp v69, v142 quad_perm:[3,3,3,3] row_mask:0xf bank_mask:0xf
	s_nop 0
	v_perm_b32 v70, v67, v66, v136
	v_perm_b32 v71, v69, v68, v137
	v_or_b32_e32 v72, v70, v71
	ds_bpermute_b32 v223, v84, v72
	s_waitcnt lgkmcnt(1)
	global_store_dword v[78:79], v222, off offset:1024
	v_mul_f32_e32 v138, v62, v116
	v_mul_f32_e32 v139, v46, v116
	v_mul_f32_e32 v140, v30, v116
	v_mul_f32_e32 v141, v14, v116
	v_mul_f32_e32 v138, 0x42000000, v138
	v_mul_f32_e32 v139, 0x42000000, v139
	v_mul_f32_e32 v140, 0x42000000, v140
	v_mul_f32_e32 v141, 0x42000000, v141
	v_med3_f32 v138, v138, s40, v212
	v_med3_f32 v139, v139, s40, v212
	v_med3_f32 v140, v140, s40, v212
	v_med3_f32 v141, v141, s40, v212
	v_cvt_pk_fp8_f32 v142, v138, v139
	v_cvt_pk_fp8_f32 v142, v140, v141 op_sel:[0,0,1]
	v_mov_b32_dpp v66, v143 quad_perm:[0,0,0,0] row_mask:0xf bank_mask:0xf
	v_mov_b32_dpp v67, v143 quad_perm:[1,1,1,1] row_mask:0xf bank_mask:0xf
	v_mov_b32_dpp v68, v143 quad_perm:[2,2,2,2] row_mask:0xf bank_mask:0xf
	v_mov_b32_dpp v69, v143 quad_perm:[3,3,3,3] row_mask:0xf bank_mask:0xf
	s_nop 0
	v_perm_b32 v70, v67, v66, v136
	v_perm_b32 v71, v69, v68, v137
	v_or_b32_e32 v72, v70, v71
	ds_bpermute_b32 v224, v84, v72
	s_waitcnt lgkmcnt(1)
	global_store_dword v[78:79], v223, off offset:2048
	v_mul_f32_e32 v138, v63, v117
	v_mul_f32_e32 v139, v47, v117
	v_mul_f32_e32 v140, v31, v117
	v_mul_f32_e32 v141, v15, v117
	v_mul_f32_e32 v138, 0x42000000, v138
	v_mul_f32_e32 v139, 0x42000000, v139
	v_mul_f32_e32 v140, 0x42000000, v140
	v_mul_f32_e32 v141, 0x42000000, v141
	v_med3_f32 v138, v138, s40, v212
	v_med3_f32 v139, v139, s40, v212
	v_med3_f32 v140, v140, s40, v212
	v_med3_f32 v141, v141, s40, v212
	v_cvt_pk_fp8_f32 v143, v138, v139
	v_cvt_pk_fp8_f32 v143, v140, v141 op_sel:[0,0,1]
	v_mov_b32_dpp v66, v142 quad_perm:[0,0,0,0] row_mask:0xf bank_mask:0xf
	v_mov_b32_dpp v67, v142 quad_perm:[1,1,1,1] row_mask:0xf bank_mask:0xf
	v_mov_b32_dpp v68, v142 quad_perm:[2,2,2,2] row_mask:0xf bank_mask:0xf
	v_mov_b32_dpp v69, v142 quad_perm:[3,3,3,3] row_mask:0xf bank_mask:0xf
	s_nop 0
	v_perm_b32 v70, v67, v66, v136
	v_perm_b32 v71, v69, v68, v137
	v_or_b32_e32 v72, v70, v71
	ds_bpermute_b32 v225, v84, v72
	s_waitcnt lgkmcnt(1)
	global_store_dword v[78:79], v224, off offset:3072
	v_mul_f32_e32 v138, v64, v118
	v_mul_f32_e32 v139, v48, v118
	v_mul_f32_e32 v140, v32, v118
	v_mul_f32_e32 v141, v16, v118
	v_mul_f32_e32 v138, 0x42000000, v138
	v_mul_f32_e32 v139, 0x42000000, v139
	v_mul_f32_e32 v140, 0x42000000, v140
	v_mul_f32_e32 v141, 0x42000000, v141
	v_med3_f32 v138, v138, s40, v212
	v_med3_f32 v139, v139, s40, v212
	v_med3_f32 v140, v140, s40, v212
	v_med3_f32 v141, v141, s40, v212
	v_cvt_pk_fp8_f32 v142, v138, v139
	v_cvt_pk_fp8_f32 v142, v140, v141 op_sel:[0,0,1]
	v_mov_b32_dpp v66, v143 quad_perm:[0,0,0,0] row_mask:0xf bank_mask:0xf
	v_mov_b32_dpp v67, v143 quad_perm:[1,1,1,1] row_mask:0xf bank_mask:0xf
	v_mov_b32_dpp v68, v143 quad_perm:[2,2,2,2] row_mask:0xf bank_mask:0xf
	v_mov_b32_dpp v69, v143 quad_perm:[3,3,3,3] row_mask:0xf bank_mask:0xf
	s_nop 0
	v_perm_b32 v70, v67, v66, v136
	v_perm_b32 v71, v69, v68, v137
	v_or_b32_e32 v72, v70, v71
	ds_bpermute_b32 v226, v84, v72
	s_waitcnt lgkmcnt(1)
	global_store_dword v[80:81], v225, off
	v_mul_f32_e32 v138, v65, v119
	v_mul_f32_e32 v139, v49, v119
	v_mul_f32_e32 v140, v33, v119
	v_mul_f32_e32 v141, v17, v119
	v_mul_f32_e32 v138, 0x42000000, v138
	v_mul_f32_e32 v139, 0x42000000, v139
	v_mul_f32_e32 v140, 0x42000000, v140
	v_mul_f32_e32 v141, 0x42000000, v141
	v_med3_f32 v138, v138, s40, v212
	v_med3_f32 v139, v139, s40, v212
	v_med3_f32 v140, v140, s40, v212
	v_med3_f32 v141, v141, s40, v212
	v_cvt_pk_fp8_f32 v143, v138, v139
	v_cvt_pk_fp8_f32 v143, v140, v141 op_sel:[0,0,1]
	v_mov_b32_dpp v66, v142 quad_perm:[0,0,0,0] row_mask:0xf bank_mask:0xf
	v_mov_b32_dpp v67, v142 quad_perm:[1,1,1,1] row_mask:0xf bank_mask:0xf
	v_mov_b32_dpp v68, v142 quad_perm:[2,2,2,2] row_mask:0xf bank_mask:0xf
	v_mov_b32_dpp v69, v142 quad_perm:[3,3,3,3] row_mask:0xf bank_mask:0xf
	s_nop 0
	v_perm_b32 v70, v67, v66, v136
	v_perm_b32 v71, v69, v68, v137
	v_or_b32_e32 v72, v70, v71
	ds_bpermute_b32 v227, v84, v72
	s_waitcnt lgkmcnt(1)
	global_store_dword v[80:81], v226, off offset:1024
	s_nop 1
	v_mov_b32_dpp v66, v143 quad_perm:[0,0,0,0] row_mask:0xf bank_mask:0xf
	v_mov_b32_dpp v67, v143 quad_perm:[1,1,1,1] row_mask:0xf bank_mask:0xf
	v_mov_b32_dpp v68, v143 quad_perm:[2,2,2,2] row_mask:0xf bank_mask:0xf
	v_mov_b32_dpp v69, v143 quad_perm:[3,3,3,3] row_mask:0xf bank_mask:0xf
	s_nop 0
	v_perm_b32 v70, v67, v66, v136
	v_perm_b32 v71, v69, v68, v137
	v_or_b32_e32 v72, v70, v71
	ds_bpermute_b32 v228, v84, v72
	s_waitcnt lgkmcnt(1)
	global_store_dword v[80:81], v227, off offset:2048
	s_waitcnt lgkmcnt(0)
	global_store_dword v[80:81], v228, off offset:3072
	s_nop 0
	s_nop 0
	s_nop 0
	s_nop 0
	s_nop 0
	s_nop 0
	s_nop 0
	s_nop 0
	s_nop 0
	s_and_b64 vcc, exec, s[28:29]
	s_cbranch_vccnz .LBB0_1718
